# v22 + non-temporal hint on the read-once f32 x/p loads of the P0 conversion fast path
# speedup vs baseline: 1.0591x; 1.0022x over previous
.Lxcv_round:
	global_load_dwordx4 v[20:23], v[12:13], off nt
	v_lshl_add_u64 v[12:13], v[12:13], 0, s[14:15]
	global_load_dwordx4 v[24:27], v[12:13], off nt
	v_lshl_add_u64 v[12:13], v[12:13], 0, s[14:15]
	global_load_dwordx4 v[28:31], v[12:13], off nt
	v_lshl_add_u64 v[12:13], v[12:13], 0, s[14:15]
	global_load_dwordx4 v[32:35], v[12:13], off nt
	v_lshl_add_u64 v[12:13], v[12:13], 0, s[14:15]
	global_load_dwordx4 v[36:39], v[12:13], off nt
	v_lshl_add_u64 v[12:13], v[12:13], 0, s[14:15]
	global_load_dwordx4 v[40:43], v[12:13], off nt
	v_lshl_add_u64 v[12:13], v[12:13], 0, s[14:15]
	global_load_dwordx4 v[44:47], v[12:13], off nt
	v_lshl_add_u64 v[12:13], v[12:13], 0, s[14:15]
	global_load_dwordx4 v[48:51], v[12:13], off nt
	v_lshl_add_u64 v[12:13], v[12:13], 0, s[14:15]
	s_waitcnt vmcnt(7)
	v_cvt_pk_bf16_f32 v52, v20, v21
	v_cvt_pk_bf16_f32 v53, v22, v23
	v_mul_f32_e32 v20, 0x41800000, v20
	v_mul_f32_e32 v21, 0x41800000, v21
	v_mul_f32_e32 v22, 0x41800000, v22
	v_mul_f32_e32 v23, 0x41800000, v23
	v_mov_b32_e32 v54, 0
	s_nop 0
	v_cvt_pk_fp8_f32 v54, v20, v21
	global_store_dwordx2 v[10:11], v[52:53], off
	v_lshl_add_u64 v[10:11], v[10:11], 0, s[10:11]
	v_cvt_pk_fp8_f32 v54, v22, v23 op_sel:[0,0,1]
	s_nop 1
	global_store_dword v[4:5], v54, off
	v_lshl_add_u64 v[4:5], v[4:5], 0, s[16:17]
	s_waitcnt vmcnt(8)
	v_cvt_pk_bf16_f32 v56, v24, v25
	v_cvt_pk_bf16_f32 v57, v26, v27
	v_mul_f32_e32 v24, 0x41800000, v24
	v_mul_f32_e32 v25, 0x41800000, v25
	v_mul_f32_e32 v26, 0x41800000, v26
	v_mul_f32_e32 v27, 0x41800000, v27
	v_mov_b32_e32 v58, 0
	s_nop 0
	v_cvt_pk_fp8_f32 v58, v24, v25
	global_store_dwordx2 v[10:11], v[56:57], off
	v_lshl_add_u64 v[10:11], v[10:11], 0, s[10:11]
	v_cvt_pk_fp8_f32 v58, v26, v27 op_sel:[0,0,1]
	s_nop 1
	global_store_dword v[4:5], v58, off
	v_lshl_add_u64 v[4:5], v[4:5], 0, s[16:17]
	s_waitcnt vmcnt(9)
	v_cvt_pk_bf16_f32 v52, v28, v29
	v_cvt_pk_bf16_f32 v53, v30, v31
	v_mul_f32_e32 v28, 0x41800000, v28
	v_mul_f32_e32 v29, 0x41800000, v29
	v_mul_f32_e32 v30, 0x41800000, v30
	v_mul_f32_e32 v31, 0x41800000, v31
	v_mov_b32_e32 v54, 0
	s_nop 0
	v_cvt_pk_fp8_f32 v54, v28, v29
	global_store_dwordx2 v[10:11], v[52:53], off
	v_lshl_add_u64 v[10:11], v[10:11], 0, s[10:11]
	v_cvt_pk_fp8_f32 v54, v30, v31 op_sel:[0,0,1]
	s_nop 1
	global_store_dword v[4:5], v54, off
	v_lshl_add_u64 v[4:5], v[4:5], 0, s[16:17]
	s_waitcnt vmcnt(10)
	v_cvt_pk_bf16_f32 v56, v32, v33
	v_cvt_pk_bf16_f32 v57, v34, v35
	v_mul_f32_e32 v32, 0x41800000, v32
	v_mul_f32_e32 v33, 0x41800000, v33
	v_mul_f32_e32 v34, 0x41800000, v34
	v_mul_f32_e32 v35, 0x41800000, v35
	v_mov_b32_e32 v58, 0
	s_nop 0
	v_cvt_pk_fp8_f32 v58, v32, v33
	global_store_dwordx2 v[10:11], v[56:57], off
	v_lshl_add_u64 v[10:11], v[10:11], 0, s[10:11]
	v_cvt_pk_fp8_f32 v58, v34, v35 op_sel:[0,0,1]
	s_nop 1
	global_store_dword v[4:5], v58, off
	v_lshl_add_u64 v[4:5], v[4:5], 0, s[16:17]
	s_waitcnt vmcnt(11)
	v_cvt_pk_bf16_f32 v52, v36, v37
	v_cvt_pk_bf16_f32 v53, v38, v39
	v_mul_f32_e32 v36, 0x41800000, v36
	v_mul_f32_e32 v37, 0x41800000, v37
	v_mul_f32_e32 v38, 0x41800000, v38
	v_mul_f32_e32 v39, 0x41800000, v39
	v_mov_b32_e32 v54, 0
	s_nop 0
	v_cvt_pk_fp8_f32 v54, v36, v37
	global_store_dwordx2 v[10:11], v[52:53], off
	v_lshl_add_u64 v[10:11], v[10:11], 0, s[10:11]
	v_cvt_pk_fp8_f32 v54, v38, v39 op_sel:[0,0,1]
	s_nop 1
	global_store_dword v[4:5], v54, off
	v_lshl_add_u64 v[4:5], v[4:5], 0, s[16:17]
	s_waitcnt vmcnt(12)
	v_cvt_pk_bf16_f32 v56, v40, v41
	v_cvt_pk_bf16_f32 v57, v42, v43
	v_mul_f32_e32 v40, 0x41800000, v40
	v_mul_f32_e32 v41, 0x41800000, v41
	v_mul_f32_e32 v42, 0x41800000, v42
	v_mul_f32_e32 v43, 0x41800000, v43
	v_mov_b32_e32 v58, 0
	s_nop 0
	v_cvt_pk_fp8_f32 v58, v40, v41
	global_store_dwordx2 v[10:11], v[56:57], off
	v_lshl_add_u64 v[10:11], v[10:11], 0, s[10:11]
	v_cvt_pk_fp8_f32 v58, v42, v43 op_sel:[0,0,1]
	s_nop 1
	global_store_dword v[4:5], v58, off
	v_lshl_add_u64 v[4:5], v[4:5], 0, s[16:17]
	s_waitcnt vmcnt(13)
	v_cvt_pk_bf16_f32 v52, v44, v45
	v_cvt_pk_bf16_f32 v53, v46, v47
	v_mul_f32_e32 v44, 0x41800000, v44
	v_mul_f32_e32 v45, 0x41800000, v45
	v_mul_f32_e32 v46, 0x41800000, v46
	v_mul_f32_e32 v47, 0x41800000, v47
	v_mov_b32_e32 v54, 0
	s_nop 0
	v_cvt_pk_fp8_f32 v54, v44, v45
	global_store_dwordx2 v[10:11], v[52:53], off
	v_lshl_add_u64 v[10:11], v[10:11], 0, s[10:11]
	v_cvt_pk_fp8_f32 v54, v46, v47 op_sel:[0,0,1]
	s_nop 1
	global_store_dword v[4:5], v54, off
	v_lshl_add_u64 v[4:5], v[4:5], 0, s[16:17]
	s_waitcnt vmcnt(14)
	v_cvt_pk_bf16_f32 v56, v48, v49
	v_cvt_pk_bf16_f32 v57, v50, v51
	v_mul_f32_e32 v48, 0x41800000, v48
	v_mul_f32_e32 v49, 0x41800000, v49
	v_mul_f32_e32 v50, 0x41800000, v50
	v_mul_f32_e32 v51, 0x41800000, v51
	v_mov_b32_e32 v58, 0
	s_nop 0
	v_cvt_pk_fp8_f32 v58, v48, v49
	global_store_dwordx2 v[10:11], v[56:57], off
	v_lshl_add_u64 v[10:11], v[10:11], 0, s[10:11]
	v_cvt_pk_fp8_f32 v58, v50, v51 op_sel:[0,0,1]
	s_nop 1
	global_store_dword v[4:5], v58, off
	v_lshl_add_u64 v[4:5], v[4:5], 0, s[16:17]
	s_sub_u32 s20, s20, 1
	s_cmp_lg_u32 s20, 0
	s_cbranch_scc1 .Lxcv_round
	s_load_dwordx2 s[22:23], s[8:9], 0x8
	s_mov_b64 s[24:25], 0x38000000
	v_lshl_add_u64 v[2:3], v[2:3], 0, s[24:25]
	s_waitcnt lgkmcnt(0)
	v_lshl_add_u64 v[4:5], s[22:23], 0, v[8:9]
	s_mov_b32 s20, 4
.Lpcv_round:
	global_load_dwordx4 v[20:23], v[4:5], off nt
	v_lshl_add_u64 v[4:5], v[4:5], 0, s[14:15]
	global_load_dwordx4 v[24:27], v[4:5], off nt
	v_lshl_add_u64 v[4:5], v[4:5], 0, s[14:15]
	global_load_dwordx4 v[28:31], v[4:5], off nt
	v_lshl_add_u64 v[4:5], v[4:5], 0, s[14:15]
	global_load_dwordx4 v[32:35], v[4:5], off nt
	v_lshl_add_u64 v[4:5], v[4:5], 0, s[14:15]
	global_load_dwordx4 v[36:39], v[4:5], off nt
	v_lshl_add_u64 v[4:5], v[4:5], 0, s[14:15]
	global_load_dwordx4 v[40:43], v[4:5], off nt
	v_lshl_add_u64 v[4:5], v[4:5], 0, s[14:15]
	global_load_dwordx4 v[44:47], v[4:5], off nt
	v_lshl_add_u64 v[4:5], v[4:5], 0, s[14:15]
	global_load_dwordx4 v[48:51], v[4:5], off nt
	v_lshl_add_u64 v[4:5], v[4:5], 0, s[14:15]
	s_waitcnt vmcnt(7)
	v_cvt_pk_bf16_f32 v52, v20, v21
	v_cvt_pk_bf16_f32 v53, v22, v23
	s_nop 0
	global_store_dwordx2 v[2:3], v[52:53], off
	v_lshl_add_u64 v[2:3], v[2:3], 0, s[10:11]
	s_waitcnt vmcnt(7)
	v_cvt_pk_bf16_f32 v56, v24, v25
	v_cvt_pk_bf16_f32 v57, v26, v27
	s_nop 0
	global_store_dwordx2 v[2:3], v[56:57], off
	v_lshl_add_u64 v[2:3], v[2:3], 0, s[10:11]
	s_waitcnt vmcnt(7)
	v_cvt_pk_bf16_f32 v52, v28, v29
	v_cvt_pk_bf16_f32 v53, v30, v31
	s_nop 0
	global_store_dwordx2 v[2:3], v[52:53], off
	v_lshl_add_u64 v[2:3], v[2:3], 0, s[10:11]
	s_waitcnt vmcnt(7)
	v_cvt_pk_bf16_f32 v56, v32, v33
	v_cvt_pk_bf16_f32 v57, v34, v35
	s_nop 0
	global_store_dwordx2 v[2:3], v[56:57], off
	v_lshl_add_u64 v[2:3], v[2:3], 0, s[10:11]
	s_waitcnt vmcnt(7)
	v_cvt_pk_bf16_f32 v52, v36, v37
	v_cvt_pk_bf16_f32 v53, v38, v39
	s_nop 0
	global_store_dwordx2 v[2:3], v[52:53], off
	v_lshl_add_u64 v[2:3], v[2:3], 0, s[10:11]
	s_waitcnt vmcnt(7)
	v_cvt_pk_bf16_f32 v56, v40, v41
	v_cvt_pk_bf16_f32 v57, v42, v43
	s_nop 0
	global_store_dwordx2 v[2:3], v[56:57], off
	v_lshl_add_u64 v[2:3], v[2:3], 0, s[10:11]
	s_waitcnt vmcnt(7)
	v_cvt_pk_bf16_f32 v52, v44, v45
	v_cvt_pk_bf16_f32 v53, v46, v47
	s_nop 0
	global_store_dwordx2 v[2:3], v[52:53], off
	v_lshl_add_u64 v[2:3], v[2:3], 0, s[10:11]
	s_waitcnt vmcnt(7)
	v_cvt_pk_bf16_f32 v56, v48, v49
	v_cvt_pk_bf16_f32 v57, v50, v51
	s_nop 0
	global_store_dwordx2 v[2:3], v[56:57], off
	v_lshl_add_u64 v[2:3], v[2:3], 0, s[10:11]
	s_sub_u32 s20, s20, 1
	s_cmp_lg_u32 s20, 0
	s_cbranch_scc1 .Lpcv_round
	s_branch .LBB0_571
